# same as the previous version with four wait states in front of every v_permlane32_swap
# speedup vs baseline: 1.0030x; 1.0029x over previous
.LBB0_799:
	s_ashr_i32 s4, s16, 1
	s_lshl_b32 s20, s4, 6
	s_and_b32 s17, s4, 3
	s_and_b32 s4, s20, 0xffffff00
	s_or_b32 s14, s4, s17
	s_ashr_i32 s15, s14, 31
	s_lshl_b64 s[4:5], s[14:15], 13
	v_readlane_b32 s6, v253, 22
	v_lshl_add_u64 v[20:21], v[134:135], 0, s[4:5]
	v_readlane_b32 s7, v253, 23
	s_add_u32 s4, s6, s4
	s_addc_u32 s5, s7, s5
	s_lshl_b32 s6, s16, 11
	s_and_b32 s6, s6, 0x800
	v_or_b32_e32 v36, s6, v132
	v_lshlrev_b32_e32 v2, 1, v132
	v_mov_b32_e32 v143, v3
	v_mov_b32_e32 v37, v3
	v_lshlrev_b32_e32 v36, 1, v36
	v_lshl_add_u64 v[16:17], v[20:21], 0, v[2:3]
	v_lshl_add_u64 v[32:33], v[20:21], 0, v[142:143]
	v_mov_b32_e32 v145, v3
	v_lshl_add_u64 v[38:39], s[4:5], 0, v[36:37]
	global_load_dwordx4 v[4:7], v[16:17], off
	global_load_dwordx4 v[8:11], v[16:17], off offset:32
	global_load_dwordx4 v[12:15], v[16:17], off offset:64
	v_lshl_add_u64 v[38:39], v[38:39], 0, v[144:145]
	global_load_dwordx4 v[16:19], v[16:17], off offset:96
	s_nop 0
	global_load_dwordx4 v[20:23], v[32:33], off
	global_load_dwordx4 v[24:27], v[32:33], off offset:32
	global_load_dwordx4 v[28:31], v[32:33], off offset:64
	s_nop 0
	global_load_dwordx4 v[32:35], v[32:33], off offset:96
	s_nop 0
	global_load_dwordx2 v[158:159], v[38:39], off
	global_load_dwordx2 v[154:155], v[38:39], off offset:16
	global_load_dwordx2 v[152:153], v[38:39], off offset:32
	global_load_dwordx2 v[150:151], v[38:39], off offset:48
	global_load_dwordx2 v[164:165], v[38:39], off offset:64
	global_load_dwordx2 v[162:163], v[38:39], off offset:80
	global_load_dwordx2 v[160:161], v[38:39], off offset:96
	global_load_dwordx2 v[156:157], v[38:39], off offset:112
	v_lshl_add_u64 v[146:147], v[138:139], 0, v[36:37]
	v_lshl_add_u64 v[148:149], v[140:141], 0, v[36:37]
	s_mov_b32 s15, 0
	s_waitcnt vmcnt(0)
	v_cndmask_b32_e32 v38, v4, v6, vcc
	ds_bpermute_b32 v38, v166, v38
	s_waitcnt lgkmcnt(0)
	v_cndmask_b32_e32 v92, v38, v4, vcc
	v_mov_b32_e32 v4, 0
	v_mov_b32_e32 v93, v5
	v_mov_b32_e32 v95, v7
	s_nop 3
	v_permlane32_swap_b32_e32 v93, v95
	s_nop 1
	v_cndmask_b32_e32 v94, v6, v38, vcc
	s_waitcnt lgkmcnt(0)
	v_mov_b64_e32 v[76:77], v[8:9]
	v_mov_b64_e32 v[78:79], v[10:11]
	s_nop 3
	v_permlane32_swap_b32_e32 v77, v79
	v_permlane32_swap_b32_e32 v76, v78
	s_nop 1
	s_waitcnt lgkmcnt(0)
	v_mov_b64_e32 v[84:85], v[12:13]
	v_mov_b64_e32 v[86:87], v[14:15]
	s_nop 3
	v_permlane32_swap_b32_e32 v85, v87
	v_permlane32_swap_b32_e32 v84, v86
	s_nop 1
	s_waitcnt lgkmcnt(0)
	v_mov_b64_e32 v[68:69], v[16:17]
	v_mov_b64_e32 v[70:71], v[18:19]
	s_nop 3
	v_permlane32_swap_b32_e32 v69, v71
	v_permlane32_swap_b32_e32 v68, v70
	s_nop 1
	s_waitcnt lgkmcnt(0)
	v_mov_b64_e32 v[96:97], v[20:21]
	v_mov_b64_e32 v[98:99], v[22:23]
	s_nop 3
	v_permlane32_swap_b32_e32 v97, v99
	v_permlane32_swap_b32_e32 v96, v98
	s_nop 1
	s_waitcnt lgkmcnt(0)
	v_mov_b64_e32 v[80:81], v[24:25]
	v_mov_b64_e32 v[82:83], v[26:27]
	s_nop 3
	v_permlane32_swap_b32_e32 v81, v83
	v_permlane32_swap_b32_e32 v80, v82
	s_nop 1
	s_waitcnt lgkmcnt(0)
	v_mov_b64_e32 v[88:89], v[28:29]
	v_mov_b64_e32 v[90:91], v[30:31]
	s_nop 3
	v_permlane32_swap_b32_e32 v89, v91
	v_permlane32_swap_b32_e32 v88, v90
	s_nop 1
	s_waitcnt lgkmcnt(0)
	v_mov_b64_e32 v[72:73], v[32:33]
	v_mov_b64_e32 v[74:75], v[34:35]
	s_nop 3
	v_permlane32_swap_b32_e32 v73, v75
	v_permlane32_swap_b32_e32 v72, v74
	s_nop 1
	v_mov_b32_e32 v5, v4
	v_mov_b32_e32 v6, v4
	v_mov_b32_e32 v7, v4
	v_mov_b32_e32 v8, v4
	v_mov_b32_e32 v9, v4
	v_mov_b32_e32 v10, v4
	v_mov_b32_e32 v11, v4
	v_mov_b32_e32 v12, v4
	v_mov_b32_e32 v13, v4
	v_mov_b32_e32 v14, v4
	v_mov_b32_e32 v15, v4
	v_mov_b32_e32 v16, v4
	v_mov_b32_e32 v17, v4
	v_mov_b32_e32 v18, v4
	v_mov_b32_e32 v19, v4
	v_mov_b32_e32 v20, v4
	v_mov_b32_e32 v21, v4
	v_mov_b32_e32 v22, v4
	v_mov_b32_e32 v23, v4
	v_mov_b32_e32 v24, v4
	v_mov_b32_e32 v25, v4
	v_mov_b32_e32 v26, v4
	v_mov_b32_e32 v27, v4
	v_mov_b32_e32 v28, v4
	v_mov_b32_e32 v29, v4
	v_mov_b32_e32 v30, v4
	v_mov_b32_e32 v31, v4
	v_mov_b32_e32 v32, v4
	v_mov_b32_e32 v33, v4
	v_mov_b32_e32 v34, v4
	v_mov_b32_e32 v35, v4
.LBB0_800:
	v_lshlrev_b32_e32 v36, 16, v158
	v_and_b32_e32 v37, 0xffff0000, v158
	v_lshlrev_b32_e32 v38, 16, v159
	v_and_b32_e32 v39, 0xffff0000, v159
	v_lshlrev_b32_e32 v40, 16, v154
	v_and_b32_e32 v41, 0xffff0000, v154
	v_lshlrev_b32_e32 v42, 16, v155
	v_and_b32_e32 v43, 0xffff0000, v155
	v_lshlrev_b32_e32 v44, 16, v152
	v_and_b32_e32 v45, 0xffff0000, v152
	v_lshlrev_b32_e32 v46, 16, v153
	v_and_b32_e32 v47, 0xffff0000, v153
	v_lshlrev_b32_e32 v48, 16, v150
	v_and_b32_e32 v49, 0xffff0000, v150
	v_lshlrev_b32_e32 v50, 16, v151
	v_and_b32_e32 v51, 0xffff0000, v151
	v_cvt_pk_bf16_f32 v116, -v20, -v21
	v_cvt_pk_bf16_f32 v117, -v22, -v23
	v_cvt_pk_bf16_f32 v118, -v24, -v25
	v_cvt_pk_bf16_f32 v119, -v26, -v27
	v_lshlrev_b32_e32 v52, 16, v164
	v_and_b32_e32 v53, 0xffff0000, v164
	v_mfma_f32_32x32x16_bf16 v[36:51], v[92:95], v[116:119], v[36:51]
	v_lshlrev_b32_e32 v54, 16, v165
	v_and_b32_e32 v55, 0xffff0000, v165
	v_lshlrev_b32_e32 v56, 16, v162
	v_and_b32_e32 v57, 0xffff0000, v162
	v_lshlrev_b32_e32 v58, 16, v163
	v_and_b32_e32 v59, 0xffff0000, v163
	v_lshlrev_b32_e32 v60, 16, v160
	v_and_b32_e32 v61, 0xffff0000, v160
	v_lshlrev_b32_e32 v62, 16, v161
	v_and_b32_e32 v63, 0xffff0000, v161
	v_lshlrev_b32_e32 v64, 16, v156
	v_and_b32_e32 v65, 0xffff0000, v156
	v_lshlrev_b32_e32 v66, 16, v157
	v_and_b32_e32 v67, 0xffff0000, v157
	s_add_i32 s18, s14, s15
	s_ashr_i32 s19, s18, 31
	v_mfma_f32_32x32x16_bf16 v[52:67], v[96:99], v[116:119], v[52:67]
	s_lshl_b64 s[4:5], s[18:19], 2
	v_cvt_pk_bf16_f32 v120, -v4, -v5
	v_cvt_pk_bf16_f32 v121, -v6, -v7
	v_cvt_pk_bf16_f32 v122, -v8, -v9
	v_cvt_pk_bf16_f32 v123, -v10, -v11
	s_add_u32 s8, s12, s4
	s_addc_u32 s9, s13, s5
	s_lshl_b64 s[6:7], s[18:19], 13
	v_mfma_f32_32x32x16_bf16 v[36:51], v[84:87], v[120:123], v[36:51]
	v_lshl_add_u64 v[96:97], v[136:137], 0, s[6:7]
	v_cvt_pk_bf16_f32 v124, -v28, -v29
	v_cvt_pk_bf16_f32 v125, -v30, -v31
	v_lshl_add_u64 v[150:151], v[96:97], 0, v[2:3]
	v_mfma_f32_32x32x16_bf16 v[52:67], v[88:91], v[120:123], v[52:67]
	v_cvt_pk_bf16_f32 v126, -v32, -v33
	global_load_dword v204, v3, s[8:9]
	v_lshl_add_u64 v[152:153], v[96:97], 0, v[142:143]
	global_load_dwordx4 v[96:99], v[150:151], off
	global_load_dwordx4 v[116:119], v[150:151], off offset:32
	s_add_i32 s4, s18, 4
	s_ashr_i32 s5, s4, 31
	s_lshl_b64 s[4:5], s[4:5], 13
	v_cvt_pk_bf16_f32 v127, -v34, -v35
	global_load_dwordx4 v[84:87], v[152:153], off
	global_load_dwordx4 v[128:131], v[152:153], off offset:32
	global_load_dwordx4 v[168:171], v[150:151], off offset:64
	global_load_dwordx4 v[172:175], v[150:151], off offset:96
	global_load_dwordx4 v[176:179], v[152:153], off offset:64
	global_load_dwordx4 v[180:183], v[152:153], off offset:96
	v_lshl_add_u64 v[150:151], v[134:135], 0, s[4:5]
	v_lshl_add_u64 v[88:89], v[146:147], 0, s[4:5]
	v_cvt_pk_bf16_f32 v92, -v12, -v13
	v_cvt_pk_bf16_f32 v93, -v14, -v15
	v_cvt_pk_bf16_f32 v94, -v16, -v17
	v_cvt_pk_bf16_f32 v95, -v18, -v19
	v_lshl_add_u64 v[120:121], v[150:151], 0, v[2:3]
	v_lshl_add_u64 v[196:197], v[150:151], 0, v[142:143]
	global_load_dwordx2 v[158:159], v[88:89], off
	global_load_dwordx2 v[154:155], v[88:89], off offset:16
	global_load_dwordx2 v[152:153], v[88:89], off offset:32
	v_mfma_f32_32x32x16_bf16 v[36:51], v[76:79], v[124:127], v[36:51]
	global_load_dwordx2 v[150:151], v[88:89], off offset:48
	global_load_dwordx2 v[164:165], v[88:89], off offset:64
	global_load_dwordx2 v[162:163], v[88:89], off offset:80
	global_load_dwordx2 v[160:161], v[88:89], off offset:96
	global_load_dwordx2 v[156:157], v[88:89], off offset:112
	global_load_dwordx4 v[76:79], v[120:121], off
	s_nop 0
	global_load_dwordx4 v[88:91], v[120:121], off offset:32
	v_cvt_pk_bf16_f32 v100, v20, v21
	v_cvt_pk_bf16_f32 v101, v22, v23
	v_cvt_pk_bf16_f32 v102, v4, v5
	v_cvt_pk_bf16_f32 v103, v6, v7
	v_cvt_pk_bf16_f32 v104, v24, v25
	v_cvt_pk_bf16_f32 v105, v26, v27
	v_mfma_f32_32x32x16_bf16 v[52:67], v[80:83], v[124:127], v[52:67]
	global_load_dwordx4 v[80:83], v[120:121], off offset:64
	s_nop 0
	global_load_dwordx4 v[120:123], v[120:121], off offset:96
	s_nop 0
	global_load_dwordx4 v[184:187], v[196:197], off
	global_load_dwordx4 v[188:191], v[196:197], off offset:32
	global_load_dwordx4 v[192:195], v[196:197], off offset:64
	s_nop 0
	global_load_dwordx4 v[196:199], v[196:197], off offset:96
	v_lshl_add_u64 v[206:207], v[148:149], 0, s[6:7]
	v_cvt_pk_bf16_f32 v106, v8, v9
	v_cvt_pk_bf16_f32 v107, v10, v11
	v_cvt_pk_bf16_f32 v108, v28, v29
	v_cvt_pk_bf16_f32 v109, v30, v31
	v_cvt_pk_bf16_f32 v110, v12, v13
	v_mfma_f32_32x32x16_bf16 v[36:51], v[68:71], v[92:95], v[36:51]
	v_cvt_pk_bf16_f32 v111, v14, v15
	v_cvt_pk_bf16_f32 v112, v32, v33
	v_cvt_pk_bf16_f32 v113, v34, v35
	v_cvt_pk_bf16_f32 v114, v16, v17
	v_cvt_pk_bf16_f32 v115, v18, v19
	global_store_dwordx2 v[206:207], v[100:101], off
	global_store_dwordx2 v[206:207], v[102:103], off offset:64
	global_store_dwordx2 v[206:207], v[104:105], off offset:16
	global_store_dwordx2 v[206:207], v[106:107], off offset:80
	global_store_dwordx2 v[206:207], v[108:109], off offset:32
	global_store_dwordx2 v[206:207], v[110:111], off offset:96
	global_store_dwordx2 v[206:207], v[112:113], off offset:48
	global_store_dwordx2 v[206:207], v[114:115], off offset:112
	v_mfma_f32_32x32x16_bf16 v[52:67], v[72:75], v[92:95], v[52:67]
	v_cvt_pk_bf16_f32 v36, v36, v37
	v_cvt_pk_bf16_f32 v37, v38, v39
	v_cvt_pk_bf16_f32 v39, v42, v43
	v_cvt_pk_bf16_f32 v42, v48, v49
	v_cvt_pk_bf16_f32 v38, v40, v41
	v_cvt_pk_bf16_f32 v40, v44, v45
	v_cvt_pk_bf16_f32 v43, v50, v51
	s_nop 4
	v_cvt_pk_bf16_f32 v52, v52, v53
	v_cvt_pk_bf16_f32 v53, v54, v55
	v_cvt_pk_bf16_f32 v54, v56, v57
	v_cvt_pk_bf16_f32 v44, v60, v61
	v_cvt_pk_bf16_f32 v45, v62, v63
	v_cvt_pk_bf16_f32 v41, v46, v47
	v_cvt_pk_bf16_f32 v46, v64, v65
	v_lshl_add_u64 v[208:209], v[146:147], 0, s[6:7]
	v_cvt_pk_bf16_f32 v55, v58, v59
	v_cvt_pk_bf16_f32 v47, v66, v67
	global_store_dwordx2 v[208:209], v[36:37], off
	global_store_dwordx2 v[208:209], v[52:53], off offset:64
	global_store_dwordx2 v[208:209], v[38:39], off offset:16
	global_store_dwordx2 v[208:209], v[54:55], off offset:80
	global_store_dwordx2 v[208:209], v[40:41], off offset:32
	global_store_dwordx2 v[208:209], v[44:45], off offset:96
	global_store_dwordx2 v[208:209], v[42:43], off offset:48
	global_store_dwordx2 v[208:209], v[46:47], off offset:112
	s_add_i32 s15, s15, 4
	s_cmpk_lg_i32 s15, 0xfc
	s_waitcnt vmcnt(40)
	v_pk_mul_f32 v[34:35], v[34:35], v[204:205] op_sel_hi:[1,0]
	s_waitcnt vmcnt(39)
	s_waitcnt vmcnt(38)
	v_pk_mul_f32 v[32:33], v[32:33], v[204:205] op_sel_hi:[1,0]
	v_pk_mul_f32 v[30:31], v[30:31], v[204:205] op_sel_hi:[1,0]
	v_pk_mul_f32 v[28:29], v[28:29], v[204:205] op_sel_hi:[1,0]
	s_waitcnt vmcnt(37)
	s_waitcnt vmcnt(35)
	s_waitcnt vmcnt(34)
	v_pk_mul_f32 v[26:27], v[26:27], v[204:205] op_sel_hi:[1,0]
	v_pk_mul_f32 v[24:25], v[24:25], v[204:205] op_sel_hi:[1,0]
	v_pk_mul_f32 v[22:23], v[22:23], v[204:205] op_sel_hi:[1,0]
	s_waitcnt vmcnt(23)
	v_pk_mul_f32 v[20:21], v[20:21], v[204:205] op_sel_hi:[1,0]
	v_pk_mul_f32 v[18:19], v[18:19], v[204:205] op_sel_hi:[1,0]
	v_pk_mul_f32 v[16:17], v[16:17], v[204:205] op_sel_hi:[1,0]
	s_waitcnt vmcnt(20)
	v_cndmask_b32_e32 v60, v120, v122, vcc
	v_cndmask_b32_e32 v61, v121, v123, vcc
	s_waitcnt vmcnt(19)
	v_cndmask_b32_e32 v62, v184, v186, vcc
	v_cndmask_b32_e32 v63, v185, v187, vcc
	v_pk_mul_f32 v[14:15], v[14:15], v[204:205] op_sel_hi:[1,0]
	v_pk_mul_f32 v[12:13], v[12:13], v[204:205] op_sel_hi:[1,0]
	v_pk_mul_f32 v[10:11], v[10:11], v[204:205] op_sel_hi:[1,0]
	v_pk_mul_f32 v[8:9], v[8:9], v[204:205] op_sel_hi:[1,0]
	v_pk_mul_f32 v[6:7], v[6:7], v[204:205] op_sel_hi:[1,0]
	v_pk_mul_f32 v[4:5], v[4:5], v[204:205] op_sel_hi:[1,0]
	ds_bpermute_b32 v145, v166, v60
	ds_bpermute_b32 v167, v166, v61
	ds_bpermute_b32 v203, v166, v62
	ds_bpermute_b32 v204, v166, v63
	s_waitcnt lgkmcnt(0)
	v_mov_b64_e32 v[48:49], v[96:97]
	v_mov_b64_e32 v[50:51], v[98:99]
	s_nop 3
	v_permlane32_swap_b32_e32 v49, v51
	v_permlane32_swap_b32_e32 v48, v50
	s_nop 1
	s_waitcnt lgkmcnt(0)
	v_mov_b64_e32 v[60:61], v[84:85]
	v_mov_b64_e32 v[62:63], v[86:87]
	s_nop 3
	v_permlane32_swap_b32_e32 v61, v63
	v_permlane32_swap_b32_e32 v60, v62
	s_nop 1
	v_mfma_f32_32x32x16_bf16 v[20:35], v[48:51], v[36:39], v[20:35]
	s_waitcnt lgkmcnt(0)
	v_mov_b64_e32 v[48:49], v[168:169]
	v_mov_b64_e32 v[50:51], v[170:171]
	s_nop 3
	v_permlane32_swap_b32_e32 v49, v51
	v_permlane32_swap_b32_e32 v48, v50
	s_nop 1
	v_mfma_f32_32x32x16_bf16 v[4:19], v[60:63], v[36:39], v[4:19]
	s_waitcnt lgkmcnt(0)
	v_mov_b64_e32 v[36:37], v[176:177]
	v_mov_b64_e32 v[38:39], v[178:179]
	s_nop 3
	v_permlane32_swap_b32_e32 v37, v39
	v_permlane32_swap_b32_e32 v36, v38
	s_nop 1
	v_mfma_f32_32x32x16_bf16 v[20:35], v[48:51], v[52:55], v[20:35]
	s_waitcnt vmcnt(18)
	v_mfma_f32_32x32x16_bf16 v[4:19], v[36:39], v[52:55], v[4:19]
	s_waitcnt vmcnt(17)
	v_mov_b64_e32 v[56:57], v[116:117]
	v_mov_b64_e32 v[58:59], v[118:119]
	s_nop 3
	v_permlane32_swap_b32_e32 v57, v59
	v_permlane32_swap_b32_e32 v56, v58
	s_nop 1
	s_waitcnt lgkmcnt(0)
	v_mov_b64_e32 v[64:65], v[128:129]
	v_mov_b64_e32 v[66:67], v[130:131]
	s_nop 3
	v_permlane32_swap_b32_e32 v65, v67
	v_permlane32_swap_b32_e32 v64, v66
	s_nop 1
	v_mfma_f32_32x32x16_bf16 v[20:35], v[56:59], v[40:43], v[20:35]
	v_mov_b64_e32 v[68:69], v[172:173]
	v_mov_b64_e32 v[70:71], v[174:175]
	s_nop 3
	v_permlane32_swap_b32_e32 v69, v71
	v_permlane32_swap_b32_e32 v68, v70
	s_nop 1
	s_waitcnt lgkmcnt(0)
	v_mov_b64_e32 v[60:61], v[180:181]
	v_mov_b64_e32 v[62:63], v[182:183]
	s_nop 3
	v_permlane32_swap_b32_e32 v61, v63
	v_permlane32_swap_b32_e32 v60, v62
	s_nop 1
	v_mfma_f32_32x32x16_bf16 v[4:19], v[64:67], v[40:43], v[4:19]
	s_waitcnt vmcnt(16)
	v_mov_b64_e32 v[128:129], v[76:77]
	v_mov_b64_e32 v[130:131], v[78:79]
	s_nop 3
	v_permlane32_swap_b32_e32 v129, v131
	v_permlane32_swap_b32_e32 v128, v130
	s_nop 1
	v_mfma_f32_32x32x16_bf16 v[20:35], v[68:71], v[44:47], v[20:35]
	s_waitcnt lgkmcnt(0)
	v_mov_b64_e32 v[112:113], v[88:89]
	v_mov_b64_e32 v[114:115], v[90:91]
	s_nop 3
	v_permlane32_swap_b32_e32 v113, v115
	v_permlane32_swap_b32_e32 v112, v114
	s_nop 1
	s_waitcnt lgkmcnt(0)
	v_mov_b64_e32 v[124:125], v[80:81]
	v_mov_b64_e32 v[126:127], v[82:83]
	s_nop 3
	v_permlane32_swap_b32_e32 v125, v127
	v_permlane32_swap_b32_e32 v124, v126
	s_nop 1
	v_mfma_f32_32x32x16_bf16 v[4:19], v[60:63], v[44:47], v[4:19]
	v_cndmask_b32_e32 v109, v167, v121, vcc
	v_cndmask_b32_e32 v108, v145, v120, vcc
	v_cndmask_b32_e32 v121, v204, v185, vcc
	v_cndmask_b32_e32 v120, v203, v184, vcc
	s_waitcnt lgkmcnt(0)
	v_mov_b64_e32 v[104:105], v[188:189]
	v_mov_b64_e32 v[106:107], v[190:191]
	s_nop 3
	v_permlane32_swap_b32_e32 v105, v107
	v_permlane32_swap_b32_e32 v104, v106
	s_nop 1
	s_waitcnt lgkmcnt(0)
	v_mov_b64_e32 v[116:117], v[192:193]
	v_mov_b64_e32 v[118:119], v[194:195]
	s_nop 3
	v_permlane32_swap_b32_e32 v117, v119
	v_permlane32_swap_b32_e32 v116, v118
	s_nop 1
	s_waitcnt lgkmcnt(0)
	v_mov_b64_e32 v[100:101], v[196:197]
	v_mov_b64_e32 v[102:103], v[198:199]
	s_nop 3
	v_permlane32_swap_b32_e32 v101, v103
	v_permlane32_swap_b32_e32 v100, v102
	s_nop 1
	v_cndmask_b32_e32 v111, v123, v167, vcc
	v_cndmask_b32_e32 v110, v122, v145, vcc
	v_cndmask_b32_e32 v123, v187, v204, vcc
	v_cndmask_b32_e32 v122, v186, v203, vcc
	v_mov_b64_e32 v[72:73], v[100:101]
	v_mov_b64_e32 v[88:89], v[116:117]
	v_mov_b64_e32 v[80:81], v[104:105]
	v_mov_b64_e32 v[96:97], v[120:121]
	v_mov_b64_e32 v[68:69], v[108:109]
	v_mov_b64_e32 v[84:85], v[124:125]
	v_mov_b64_e32 v[76:77], v[112:113]
	v_mov_b64_e32 v[92:93], v[128:129]
	v_mov_b64_e32 v[74:75], v[102:103]
	v_mov_b64_e32 v[90:91], v[118:119]
	v_mov_b64_e32 v[82:83], v[106:107]
	v_mov_b64_e32 v[98:99], v[122:123]
	v_mov_b64_e32 v[70:71], v[110:111]
	v_mov_b64_e32 v[86:87], v[126:127]
	v_mov_b64_e32 v[78:79], v[114:115]
	v_mov_b64_e32 v[94:95], v[130:131]
	s_cbranch_scc1 .LBB0_800
	v_cvt_pk_bf16_f32 v70, v20, v21
	v_cvt_pk_bf16_f32 v20, -v20, -v21
	v_cvt_pk_bf16_f32 v71, v22, v23
	v_cvt_pk_bf16_f32 v21, -v22, -v23
	v_cvt_pk_bf16_f32 v22, -v24, -v25
	v_lshlrev_b32_e32 v52, 16, v158
	v_and_b32_e32 v53, 0xffff0000, v158
	v_lshlrev_b32_e32 v54, 16, v159
	v_and_b32_e32 v55, 0xffff0000, v159
	v_lshlrev_b32_e32 v56, 16, v154
	v_and_b32_e32 v57, 0xffff0000, v154
	v_lshlrev_b32_e32 v58, 16, v155
	v_and_b32_e32 v59, 0xffff0000, v155
	v_lshlrev_b32_e32 v60, 16, v152
	v_and_b32_e32 v61, 0xffff0000, v152
	v_lshlrev_b32_e32 v62, 16, v153
	v_and_b32_e32 v63, 0xffff0000, v153
	v_lshlrev_b32_e32 v64, 16, v150
	v_and_b32_e32 v65, 0xffff0000, v150
	v_lshlrev_b32_e32 v66, 16, v151
	v_and_b32_e32 v67, 0xffff0000, v151
	v_cvt_pk_bf16_f32 v23, -v26, -v27
	v_lshlrev_b32_e32 v36, 16, v164
	v_and_b32_e32 v37, 0xffff0000, v164
	v_lshlrev_b32_e32 v38, 16, v165
	v_and_b32_e32 v39, 0xffff0000, v165
	v_lshlrev_b32_e32 v40, 16, v162
	v_and_b32_e32 v41, 0xffff0000, v162
	v_lshlrev_b32_e32 v42, 16, v163
	v_and_b32_e32 v43, 0xffff0000, v163
	v_lshlrev_b32_e32 v44, 16, v160
	v_and_b32_e32 v45, 0xffff0000, v160
	v_lshlrev_b32_e32 v46, 16, v161
	v_and_b32_e32 v47, 0xffff0000, v161
	v_lshlrev_b32_e32 v48, 16, v156
	v_and_b32_e32 v49, 0xffff0000, v156
	v_lshlrev_b32_e32 v50, 16, v157
	v_and_b32_e32 v51, 0xffff0000, v157
	v_mfma_f32_32x32x16_bf16 v[52:67], v[128:131], v[20:23], v[52:67]
	v_cvt_pk_bf16_f32 v72, v4, v5
	v_cvt_pk_bf16_f32 v4, -v4, -v5
	v_cvt_pk_bf16_f32 v73, v6, v7
	v_mfma_f32_32x32x16_bf16 v[36:51], v[120:123], v[20:23], v[36:51]
	v_cvt_pk_bf16_f32 v5, -v6, -v7
	v_cvt_pk_bf16_f32 v6, -v8, -v9
	v_cvt_pk_bf16_f32 v7, -v10, -v11
	s_or_b32 s4, s20, s17
	v_mfma_f32_32x32x16_bf16 v[52:67], v[124:127], v[4:7], v[52:67]
	s_or_b32 s4, s4, 0xfc
	s_ashr_i32 s5, s4, 31
	s_lshl_b64 s[14:15], s[4:5], 13
	v_lshl_add_u64 v[68:69], v[148:149], 0, s[14:15]
	global_store_dwordx2 v[68:69], v[70:71], off
	global_store_dwordx2 v[68:69], v[72:73], off offset:64
	v_cvt_pk_bf16_f32 v72, v8, v9
	v_mfma_f32_32x32x16_bf16 v[36:51], v[116:119], v[4:7], v[36:51]
	v_cvt_pk_bf16_f32 v4, -v28, -v29
	v_cvt_pk_bf16_f32 v5, -v30, -v31
	v_cvt_pk_bf16_f32 v6, -v32, -v33
	v_cvt_pk_bf16_f32 v7, -v34, -v35
	v_cvt_pk_bf16_f32 v8, -v12, -v13
	v_mfma_f32_32x32x16_bf16 v[52:67], v[112:115], v[4:7], v[52:67]
	v_cvt_pk_bf16_f32 v73, v10, v11
	v_cvt_pk_bf16_f32 v9, -v14, -v15
	v_cvt_pk_bf16_f32 v10, -v16, -v17
	v_mfma_f32_32x32x16_bf16 v[36:51], v[104:107], v[4:7], v[36:51]
	v_xor_b32_e32 v2, 0x80000000, v18
	v_xor_b32_e32 v11, 0x80000000, v19
	v_cvt_pk_bf16_f32 v11, v2, v11
	v_cvt_pk_bf16_f32 v70, v24, v25
	v_cvt_pk_bf16_f32 v71, v26, v27
	global_store_dwordx2 v[68:69], v[70:71], off offset:16
	global_store_dwordx2 v[68:69], v[72:73], off offset:80
	v_cvt_pk_bf16_f32 v70, v28, v29
	v_mfma_f32_32x32x16_bf16 v[52:67], v[108:111], v[8:11], v[52:67]
	v_cvt_pk_bf16_f32 v71, v30, v31
	v_cvt_pk_bf16_f32 v72, v12, v13
	v_cvt_pk_bf16_f32 v73, v14, v15
	global_store_dwordx2 v[68:69], v[70:71], off offset:32
	global_store_dwordx2 v[68:69], v[72:73], off offset:96
	v_cvt_pk_bf16_f32 v70, v32, v33
	v_cvt_pk_bf16_f32 v71, v34, v35
	v_lshl_add_u64 v[4:5], v[146:147], 0, s[14:15]
	v_mfma_f32_32x32x16_bf16 v[36:51], v[100:103], v[8:11], v[36:51]
	s_nop 2
	v_cvt_pk_bf16_f32 v6, v52, v53
	v_cvt_pk_bf16_f32 v7, v54, v55
	v_cvt_pk_bf16_f32 v72, v16, v17
	v_cvt_pk_bf16_f32 v73, v18, v19
	global_store_dwordx2 v[68:69], v[70:71], off offset:48
	global_store_dwordx2 v[68:69], v[72:73], off offset:112
	s_add_i32 s16, s16, s54
	s_cmp_lt_i32 s16, 64
	s_nop 0
	v_cvt_pk_bf16_f32 v8, v36, v37
	v_cvt_pk_bf16_f32 v9, v38, v39
	global_store_dwordx2 v[4:5], v[6:7], off
	global_store_dwordx2 v[4:5], v[8:9], off offset:64
	v_cvt_pk_bf16_f32 v6, v56, v57
	v_cvt_pk_bf16_f32 v7, v58, v59
	v_cvt_pk_bf16_f32 v8, v40, v41
	v_cvt_pk_bf16_f32 v9, v42, v43
	global_store_dwordx2 v[4:5], v[6:7], off offset:16
	global_store_dwordx2 v[4:5], v[8:9], off offset:80
	v_cvt_pk_bf16_f32 v6, v60, v61
	v_cvt_pk_bf16_f32 v7, v62, v63
	v_cvt_pk_bf16_f32 v8, v44, v45
	v_cvt_pk_bf16_f32 v9, v46, v47
	global_store_dwordx2 v[4:5], v[6:7], off offset:32
	global_store_dwordx2 v[4:5], v[8:9], off offset:96
	v_cvt_pk_bf16_f32 v6, v64, v65
	v_cvt_pk_bf16_f32 v7, v66, v67
	v_cvt_pk_bf16_f32 v8, v48, v49
	v_cvt_pk_bf16_f32 v9, v50, v51
	global_store_dwordx2 v[4:5], v[6:7], off offset:48
	global_store_dwordx2 v[4:5], v[8:9], off offset:112
	s_cbranch_scc1 .LBB0_799

.LBB0_827:
	s_nop 10
	v_max3_f32 v2, v36, v37, v38
	v_max3_f32 v152, v52, v53, v54
	v_max3_f32 v2, v2, v39, v40
	v_max3_f32 v152, v152, v55, v56
	v_max3_f32 v2, v2, v41, v42
	v_max3_f32 v152, v152, v57, v58
	v_max3_f32 v2, v2, v43, v44
	v_max3_f32 v152, v152, v59, v60
	v_max3_f32 v2, v2, v45, v46
	v_max3_f32 v152, v152, v61, v62
	v_max3_f32 v2, v2, v47, v48
	v_max3_f32 v152, v152, v63, v64
	v_max3_f32 v2, v2, v49, v50
	v_max3_f32 v152, v152, v65, v66
	v_max3_f32 v2, v2, v51, v67
	v_max_f32_e32 v2, v2, v152
	v_and_b32_e32 v153, 64, v250
	v_xor_b32_e32 v152, 32, v250
	v_add_u32_e32 v153, 64, v153
	v_cmp_lt_i32_e32 vcc, v152, v153
	s_nop 1
	v_cndmask_b32_e32 v152, v250, v152, vcc
	v_lshlrev_b32_e32 v152, 2, v152
	v_mov_b32_e32 v153, v2
	s_nop 3
	v_permlane32_swap_b32_e32 v2, v153
	s_nop 1
	s_waitcnt lgkmcnt(0)
	v_max3_f32 v2, v151, v2, v153
	v_cmp_gt_f32_e32 vcc, v2, v151
	s_cbranch_vccz .LBB0_829
	v_sub_f32_e32 v151, v151, v2
	v_mul_f32_e32 v151, 0x3e16c740, v151
	v_exp_f32_e32 v154, v151
	s_nop 0
	v_mul_f32_e32 v135, v135, v154
	v_pk_mul_f32 v[34:35], v[34:35], v[154:155] op_sel_hi:[1,0]
	v_pk_mul_f32 v[32:33], v[32:33], v[154:155] op_sel_hi:[1,0]
	v_pk_mul_f32 v[30:31], v[30:31], v[154:155] op_sel_hi:[1,0]
	v_pk_mul_f32 v[28:29], v[28:29], v[154:155] op_sel_hi:[1,0]
	v_pk_mul_f32 v[26:27], v[26:27], v[154:155] op_sel_hi:[1,0]
	v_pk_mul_f32 v[24:25], v[24:25], v[154:155] op_sel_hi:[1,0]
	v_pk_mul_f32 v[22:23], v[22:23], v[154:155] op_sel_hi:[1,0]
	v_pk_mul_f32 v[20:21], v[20:21], v[154:155] op_sel_hi:[1,0]
	v_pk_mul_f32 v[18:19], v[18:19], v[154:155] op_sel_hi:[1,0]
	v_pk_mul_f32 v[16:17], v[16:17], v[154:155] op_sel_hi:[1,0]
	v_pk_mul_f32 v[14:15], v[14:15], v[154:155] op_sel_hi:[1,0]
	v_pk_mul_f32 v[12:13], v[12:13], v[154:155] op_sel_hi:[1,0]
	v_pk_mul_f32 v[10:11], v[10:11], v[154:155] op_sel_hi:[1,0]
	v_pk_mul_f32 v[8:9], v[8:9], v[154:155] op_sel_hi:[1,0]
	v_pk_mul_f32 v[6:7], v[6:7], v[154:155] op_sel_hi:[1,0]
	v_pk_mul_f32 v[4:5], v[4:5], v[154:155] op_sel_hi:[1,0]

.LBB0_843:
	s_nop 10
	v_max3_f32 v69, v36, v37, v38
	v_max3_f32 v68, v52, v53, v54
	v_max3_f32 v69, v69, v39, v40
	v_max3_f32 v68, v68, v55, v56
	v_max3_f32 v69, v69, v41, v42
	v_max3_f32 v68, v68, v57, v58
	v_max3_f32 v69, v69, v43, v44
	v_max3_f32 v68, v68, v59, v60
	v_max3_f32 v69, v69, v45, v46
	v_max3_f32 v68, v68, v61, v62
	v_max3_f32 v69, v69, v47, v48
	v_max3_f32 v68, v68, v63, v64
	v_max3_f32 v69, v69, v49, v50
	v_max3_f32 v68, v68, v65, v66
	v_max3_f32 v69, v69, v51, v67
	v_max_f32_e32 v69, v69, v68
	v_and_b32_e32 v70, 64, v250
	v_xor_b32_e32 v68, 32, v250
	v_add_u32_e32 v70, 64, v70
	v_cmp_lt_i32_e32 vcc, v68, v70
	s_nop 1
	v_cndmask_b32_e32 v68, v250, v68, vcc
	v_lshlrev_b32_e32 v68, 2, v68
	v_mov_b32_e32 v70, v69
	s_nop 3
	v_permlane32_swap_b32_e32 v69, v70
	s_nop 1
	s_waitcnt lgkmcnt(0)
	v_max3_f32 v69, v2, v69, v70
	v_cmp_gt_f32_e32 vcc, v69, v2
	s_cbranch_vccz .LBB0_845
	v_sub_f32_e32 v2, v2, v69
	v_mul_f32_e32 v2, 0x3e16c740, v2
	v_exp_f32_e32 v2, v2
	s_nop 0
	v_mul_f32_e32 v135, v135, v2
	v_pk_mul_f32 v[34:35], v[34:35], v[2:3] op_sel_hi:[1,0]
	v_pk_mul_f32 v[32:33], v[32:33], v[2:3] op_sel_hi:[1,0]
	v_pk_mul_f32 v[30:31], v[30:31], v[2:3] op_sel_hi:[1,0]
	v_pk_mul_f32 v[28:29], v[28:29], v[2:3] op_sel_hi:[1,0]
	v_pk_mul_f32 v[26:27], v[26:27], v[2:3] op_sel_hi:[1,0]
	v_pk_mul_f32 v[24:25], v[24:25], v[2:3] op_sel_hi:[1,0]
	v_pk_mul_f32 v[22:23], v[22:23], v[2:3] op_sel_hi:[1,0]
	v_pk_mul_f32 v[20:21], v[20:21], v[2:3] op_sel_hi:[1,0]
	v_pk_mul_f32 v[18:19], v[18:19], v[2:3] op_sel_hi:[1,0]
	v_pk_mul_f32 v[16:17], v[16:17], v[2:3] op_sel_hi:[1,0]
	v_pk_mul_f32 v[14:15], v[14:15], v[2:3] op_sel_hi:[1,0]
	v_pk_mul_f32 v[12:13], v[12:13], v[2:3] op_sel_hi:[1,0]
	v_pk_mul_f32 v[10:11], v[10:11], v[2:3] op_sel_hi:[1,0]
	v_pk_mul_f32 v[8:9], v[8:9], v[2:3] op_sel_hi:[1,0]
	v_pk_mul_f32 v[6:7], v[6:7], v[2:3] op_sel_hi:[1,0]
	v_pk_mul_f32 v[4:5], v[4:5], v[2:3] op_sel_hi:[1,0]
